# MoE stagger group = parity of wave-id bits 0 and 2 (waves 1,3,4,6 run the weight-tile block first) instead of odd waves
# speedup vs baseline: 1.0053x; 1.0053x over previous
.LBB0_1013:
	s_or_b64 exec, exec, s[34:35]
	s_waitcnt vmcnt(0)
	v_lshlrev_b32_e32 v3, 11, v3
	v_and_b32_e32 v3, 0x7fff800, v3
	s_lshl_b64 s[34:35], s[10:11], 22
	s_add_u32 s10, s12, s34
	s_addc_u32 s52, s13, s35
	s_lshl_b32 s34, s36, 9
	s_lshl_b32 s35, s46, 6
	s_sub_i32 s34, s35, s34
	s_ashr_i32 s35, s34, 31
	s_lshl_b64 s[36:37], s[34:35], 2
	s_add_u32 s36, s10, s36
	s_addc_u32 s37, s52, s37
	v_or_b32_e32 v146, v3, v1
	s_waitcnt lgkmcnt(0)
	v_readfirstlane_b32 s51, v2
	v_lshl_add_u64 v[2:3], s[36:37], 0, v[152:153]
	v_lshl_add_u64 v[156:157], v[2:3], 0, v[148:149]
	s_mov_b64 s[36:37], -1
	s_cmp_ge_i32 s38, s50
	v_lshl_add_u64 v[132:133], v[156:157], 0, s[22:23]
	v_lshl_add_u64 v[130:131], v[156:157], 0, s[24:25]
	v_lshl_add_u64 v[134:135], v[156:157], 0, s[26:27]
	v_lshl_add_u64 v[138:139], v[156:157], 0, s[28:29]
	v_lshl_add_u64 v[142:143], v[156:157], 0, s[30:31]
	s_cbranch_scc0 .LBB0_1017
	global_load_dwordx4 v[2:5], v[156:157], off sc1 nt
	s_mov_b32 m0, s39
	global_load_dwordx4 v[6:9], v[132:133], off sc1 nt
	v_lshl_add_u64 v[50:51], s[14:15], 0, v[146:147]
	global_load_lds_dwordx4 v146, s[14:15]
	global_load_dwordx4 v[34:37], v[130:131], off sc1 nt
	global_load_dwordx4 v[38:41], v[134:135], off sc1 nt
	s_mov_b32 m0, s40
	s_nop 0
	global_load_lds_dwordx4 v146, s[16:17]
	s_waitcnt vmcnt(4)
	s_nop 0
	v_cvt_pk_bf16_f32 v2, v2, v6
	ds_write_b32 v169, v2 offset:49152
	v_cvt_pk_bf16_f32 v2, v3, v7
	ds_write_b32 v169, v2 offset:49216
	v_cvt_pk_bf16_f32 v2, v4, v8
	ds_write_b32 v169, v2 offset:49280
	v_cvt_pk_bf16_f32 v2, v5, v9
	ds_write_b32 v169, v2 offset:49344
	global_load_dwordx4 v[42:45], v[138:139], off sc1 nt
	global_load_dwordx4 v[46:49], v[142:143], off sc1 nt
	s_waitcnt vmcnt(5)
	s_mov_b32 m0, s41
	s_waitcnt lgkmcnt(0)
	s_barrier
	global_load_lds_dwordx4 v146, s[18:19]
	v_mov_b32_e32 v2, 0
	s_mov_b32 s37, -2
	s_movk_i32 s36, 0x80
	v_mov_b32_e32 v3, v2
	v_mov_b32_e32 v4, v2
	v_mov_b32_e32 v5, v2
	v_mov_b32_e32 v6, v2
	v_mov_b32_e32 v7, v2
	v_mov_b32_e32 v8, v2
	v_mov_b32_e32 v9, v2
	v_mov_b32_e32 v10, v2
	v_mov_b32_e32 v11, v2
	v_mov_b32_e32 v12, v2
	v_mov_b32_e32 v13, v2
	v_mov_b32_e32 v14, v2
	v_mov_b32_e32 v15, v2
	v_mov_b32_e32 v16, v2
	v_mov_b32_e32 v17, v2
	v_mov_b32_e32 v66, v2
	v_mov_b32_e32 v67, v2
	v_mov_b32_e32 v68, v2
	v_mov_b32_e32 v69, v2
	v_mov_b32_e32 v70, v2
	v_mov_b32_e32 v71, v2
	v_mov_b32_e32 v72, v2
	v_mov_b32_e32 v73, v2
	v_mov_b32_e32 v74, v2
	v_mov_b32_e32 v75, v2
	v_mov_b32_e32 v76, v2
	v_mov_b32_e32 v77, v2
	v_mov_b32_e32 v78, v2
	v_mov_b32_e32 v79, v2
	v_mov_b32_e32 v80, v2
	v_mov_b32_e32 v81, v2
	v_mov_b32_e32 v18, v2
	v_mov_b32_e32 v19, v2
	v_mov_b32_e32 v20, v2
	v_mov_b32_e32 v21, v2
	v_mov_b32_e32 v22, v2
	v_mov_b32_e32 v23, v2
	v_mov_b32_e32 v24, v2
	v_mov_b32_e32 v25, v2
	v_mov_b32_e32 v26, v2
	v_mov_b32_e32 v27, v2
	v_mov_b32_e32 v28, v2
	v_mov_b32_e32 v29, v2
	v_mov_b32_e32 v30, v2
	v_mov_b32_e32 v31, v2
	v_mov_b32_e32 v32, v2
	v_mov_b32_e32 v33, v2
	v_mov_b32_e32 v114, v2
	v_mov_b32_e32 v115, v2
	v_mov_b32_e32 v116, v2
	v_mov_b32_e32 v117, v2
	v_mov_b32_e32 v118, v2
	v_mov_b32_e32 v119, v2
	v_mov_b32_e32 v120, v2
	v_mov_b32_e32 v121, v2
	v_mov_b32_e32 v122, v2
	v_mov_b32_e32 v123, v2
	v_mov_b32_e32 v124, v2
	v_mov_b32_e32 v125, v2
	v_mov_b32_e32 v126, v2
	v_mov_b32_e32 v127, v2
	v_mov_b32_e32 v128, v2
	v_mov_b32_e32 v129, v2
	v_readfirstlane_b32 s98, v250
	s_lshr_b32 s99, s98, 2
	s_xor_b32 s98, s98, s99
	s_bitcmp1_b32 s98, 6
	s_cbranch_scc1 .Lmoe_B_1015

.LBB0_1017:
	v_mov_b32_e32 v97, 0
	s_and_b64 vcc, exec, s[36:37]
	v_mov_b32_e32 v96, v97
	v_mov_b32_e32 v95, v97
	v_mov_b32_e32 v94, v97
	v_mov_b32_e32 v93, v97
	v_mov_b32_e32 v92, v97
	v_mov_b32_e32 v91, v97
	v_mov_b32_e32 v90, v97
	v_mov_b32_e32 v89, v97
	v_mov_b32_e32 v88, v97
	v_mov_b32_e32 v87, v97
	v_mov_b32_e32 v86, v97
	v_mov_b32_e32 v85, v97
	v_mov_b32_e32 v84, v97
	v_mov_b32_e32 v83, v97
	v_mov_b32_e32 v82, v97
	v_mov_b32_e32 v65, v97
	v_mov_b32_e32 v64, v97
	v_mov_b32_e32 v63, v97
	v_mov_b32_e32 v62, v97
	v_mov_b32_e32 v61, v97
	v_mov_b32_e32 v60, v97
	v_mov_b32_e32 v59, v97
	v_mov_b32_e32 v58, v97
	v_mov_b32_e32 v57, v97
	v_mov_b32_e32 v56, v97
	v_mov_b32_e32 v55, v97
	v_mov_b32_e32 v54, v97
	v_mov_b32_e32 v53, v97
	v_mov_b32_e32 v52, v97
	v_mov_b32_e32 v51, v97
	v_mov_b32_e32 v50, v97
	v_mov_b32_e32 v113, v97
	v_mov_b32_e32 v112, v97
	v_mov_b32_e32 v111, v97
	v_mov_b32_e32 v110, v97
	v_mov_b32_e32 v109, v97
	v_mov_b32_e32 v108, v97
	v_mov_b32_e32 v107, v97
	v_mov_b32_e32 v106, v97
	v_mov_b32_e32 v105, v97
	v_mov_b32_e32 v104, v97
	v_mov_b32_e32 v103, v97
	v_mov_b32_e32 v102, v97
	v_mov_b32_e32 v101, v97
	v_mov_b32_e32 v100, v97
	v_mov_b32_e32 v99, v97
	v_mov_b32_e32 v98, v97
	v_mov_b32_e32 v49, v97
	v_mov_b32_e32 v48, v97
	v_mov_b32_e32 v47, v97
	v_mov_b32_e32 v46, v97
	v_mov_b32_e32 v45, v97
	v_mov_b32_e32 v44, v97
	v_mov_b32_e32 v43, v97
	v_mov_b32_e32 v42, v97
	v_mov_b32_e32 v41, v97
	v_mov_b32_e32 v40, v97
	v_mov_b32_e32 v39, v97
	v_mov_b32_e32 v38, v97
	v_mov_b32_e32 v37, v97
	v_mov_b32_e32 v36, v97
	v_mov_b32_e32 v35, v97
	v_mov_b32_e32 v34, v97
	s_cbranch_vccz .LBB0_1021
	global_load_dwordx4 v[2:5], v[156:157], off sc1 nt
	s_mov_b32 m0, s39
	global_load_dwordx4 v[6:9], v[132:133], off sc1 nt
	v_or_b32_e32 v158, v136, v1
	global_load_lds_dwordx4 v146, s[14:15]
	s_mov_b32 m0, s42
	v_mov_b32_e32 v159, v147
	global_load_lds_dwordx4 v158, s[14:15]
	global_load_dwordx4 v[130:133], v[130:131], off sc1 nt
	global_load_dwordx4 v[134:137], v[134:135], off sc1 nt
	s_mov_b32 m0, s40
	s_nop 0
	global_load_lds_dwordx4 v146, s[16:17]
	s_mov_b32 m0, s43
	s_nop 0
	global_load_lds_dwordx4 v158, s[16:17]
	s_waitcnt vmcnt(6)
	s_nop 0
	v_cvt_pk_bf16_f32 v2, v2, v6
	ds_write_b32 v169, v2 offset:49152
	v_cvt_pk_bf16_f32 v2, v3, v7
	ds_write_b32 v169, v2 offset:49216
	v_cvt_pk_bf16_f32 v2, v4, v8
	ds_write_b32 v169, v2 offset:49280
	v_cvt_pk_bf16_f32 v2, v5, v9
	ds_write_b32 v169, v2 offset:49344
	global_load_dwordx4 v[138:141], v[138:139], off sc1 nt
	global_load_dwordx4 v[142:145], v[142:143], off sc1 nt
	s_waitcnt vmcnt(6)
	s_mov_b32 m0, s41
	s_waitcnt lgkmcnt(0)
	s_barrier
	global_load_lds_dwordx4 v146, s[18:19]
	s_mov_b32 m0, s44
	v_mov_b32_e32 v34, 0
	global_load_lds_dwordx4 v158, s[18:19]
	s_mov_b32 s37, -2
	s_movk_i32 s36, 0x80
	v_mov_b32_e32 v35, v34
	v_mov_b32_e32 v36, v34
	v_mov_b32_e32 v37, v34
	v_mov_b32_e32 v38, v34
	v_mov_b32_e32 v39, v34
	v_mov_b32_e32 v40, v34
	v_mov_b32_e32 v41, v34
	v_mov_b32_e32 v42, v34
	v_mov_b32_e32 v43, v34
	v_mov_b32_e32 v44, v34
	v_mov_b32_e32 v45, v34
	v_mov_b32_e32 v46, v34
	v_mov_b32_e32 v47, v34
	v_mov_b32_e32 v48, v34
	v_mov_b32_e32 v49, v34
	v_mov_b32_e32 v98, v34
	v_mov_b32_e32 v99, v34
	v_mov_b32_e32 v100, v34
	v_mov_b32_e32 v101, v34
	v_mov_b32_e32 v102, v34
	v_mov_b32_e32 v103, v34
	v_mov_b32_e32 v104, v34
	v_mov_b32_e32 v105, v34
	v_mov_b32_e32 v106, v34
	v_mov_b32_e32 v107, v34
	v_mov_b32_e32 v108, v34
	v_mov_b32_e32 v109, v34
	v_mov_b32_e32 v110, v34
	v_mov_b32_e32 v111, v34
	v_mov_b32_e32 v112, v34
	v_mov_b32_e32 v113, v34
	v_mov_b32_e32 v50, v34
	v_mov_b32_e32 v51, v34
	v_mov_b32_e32 v52, v34
	v_mov_b32_e32 v53, v34
	v_mov_b32_e32 v54, v34
	v_mov_b32_e32 v55, v34
	v_mov_b32_e32 v56, v34
	v_mov_b32_e32 v57, v34
	v_mov_b32_e32 v58, v34
	v_mov_b32_e32 v59, v34
	v_mov_b32_e32 v60, v34
	v_mov_b32_e32 v61, v34
	v_mov_b32_e32 v62, v34
	v_mov_b32_e32 v63, v34
	v_mov_b32_e32 v64, v34
	v_mov_b32_e32 v65, v34
	v_mov_b32_e32 v82, v34
	v_mov_b32_e32 v83, v34
	v_mov_b32_e32 v84, v34
	v_mov_b32_e32 v85, v34
	v_mov_b32_e32 v86, v34
	v_mov_b32_e32 v87, v34
	v_mov_b32_e32 v88, v34
	v_mov_b32_e32 v89, v34
	v_mov_b32_e32 v90, v34
	v_mov_b32_e32 v91, v34
	v_mov_b32_e32 v92, v34
	v_mov_b32_e32 v93, v34
	v_mov_b32_e32 v94, v34
	v_mov_b32_e32 v95, v34
	v_mov_b32_e32 v96, v34
	v_mov_b32_e32 v97, v34
	v_mov_b32_e32 v2, v34
	v_mov_b32_e32 v3, v34
	v_mov_b32_e32 v4, v34
	v_mov_b32_e32 v5, v34
	v_mov_b32_e32 v6, v34
	v_mov_b32_e32 v7, v34
	v_mov_b32_e32 v8, v34
	v_mov_b32_e32 v9, v34
	v_mov_b32_e32 v10, v34
	v_mov_b32_e32 v11, v34
	v_mov_b32_e32 v12, v34
	v_mov_b32_e32 v13, v34
	v_mov_b32_e32 v14, v34
	v_mov_b32_e32 v15, v34
	v_mov_b32_e32 v16, v34
	v_mov_b32_e32 v17, v34
	v_mov_b32_e32 v66, v34
	v_mov_b32_e32 v67, v34
	v_mov_b32_e32 v68, v34
	v_mov_b32_e32 v69, v34
	v_mov_b32_e32 v70, v34
	v_mov_b32_e32 v71, v34
	v_mov_b32_e32 v72, v34
	v_mov_b32_e32 v73, v34
	v_mov_b32_e32 v74, v34
	v_mov_b32_e32 v75, v34
	v_mov_b32_e32 v76, v34
	v_mov_b32_e32 v77, v34
	v_mov_b32_e32 v78, v34
	v_mov_b32_e32 v79, v34
	v_mov_b32_e32 v80, v34
	v_mov_b32_e32 v81, v34
	v_mov_b32_e32 v18, v34
	v_mov_b32_e32 v19, v34
	v_mov_b32_e32 v20, v34
	v_mov_b32_e32 v21, v34
	v_mov_b32_e32 v22, v34
	v_mov_b32_e32 v23, v34
	v_mov_b32_e32 v24, v34
	v_mov_b32_e32 v25, v34
	v_mov_b32_e32 v26, v34
	v_mov_b32_e32 v27, v34
	v_mov_b32_e32 v28, v34
	v_mov_b32_e32 v29, v34
	v_mov_b32_e32 v30, v34
	v_mov_b32_e32 v31, v34
	v_mov_b32_e32 v32, v34
	v_mov_b32_e32 v33, v34
	v_mov_b32_e32 v114, v34
	v_mov_b32_e32 v115, v34
	v_mov_b32_e32 v116, v34
	v_mov_b32_e32 v117, v34
	v_mov_b32_e32 v118, v34
	v_mov_b32_e32 v119, v34
	v_mov_b32_e32 v120, v34
	v_mov_b32_e32 v121, v34
	v_mov_b32_e32 v122, v34
	v_mov_b32_e32 v123, v34
	v_mov_b32_e32 v124, v34
	v_mov_b32_e32 v125, v34
	v_mov_b32_e32 v126, v34
	v_mov_b32_e32 v127, v34
	v_mov_b32_e32 v128, v34
	v_mov_b32_e32 v129, v34
	v_readfirstlane_b32 s98, v250
	s_lshr_b32 s99, s98, 2
	s_xor_b32 s98, s98, s99
	s_bitcmp1_b32 s98, 6
	s_cbranch_scc1 .Lmoe_B_1019

.Lp9pf_n1:
	s_or_b64 exec, exec, s[100:101]
	s_waitcnt vmcnt(4)
	s_nop 0
	v_cvt_pk_bf16_f32 v2, v2, v6
	ds_write_b32 v167, v2 offset:49152
	v_cvt_pk_bf16_f32 v2, v3, v7
	ds_write_b32 v167, v2 offset:49216
	v_cvt_pk_bf16_f32 v2, v4, v8
	ds_write_b32 v167, v2 offset:49280
	v_cvt_pk_bf16_f32 v2, v5, v9
	ds_write_b32 v167, v2 offset:49344
	global_load_dwordx4 v[74:77], v[138:139], off sc1 nt
	global_load_dwordx4 v[78:81], v[142:143], off sc1 nt
	s_waitcnt vmcnt(5)
	s_mov_b32 m0, s41
	s_waitcnt lgkmcnt(0)
	s_barrier
	global_load_lds_dwordx4 v146, s[16:17]
	v_mov_b32_e32 v2, 0
	s_mov_b32 s36, -2
	s_movk_i32 s35, 0x80
	v_mov_b32_e32 v3, v2
	v_mov_b32_e32 v4, v2
	v_mov_b32_e32 v5, v2
	v_mov_b32_e32 v6, v2
	v_mov_b32_e32 v7, v2
	v_mov_b32_e32 v8, v2
	v_mov_b32_e32 v9, v2
	v_mov_b32_e32 v10, v2
	v_mov_b32_e32 v11, v2
	v_mov_b32_e32 v12, v2
	v_mov_b32_e32 v13, v2
	v_mov_b32_e32 v14, v2
	v_mov_b32_e32 v15, v2
	v_mov_b32_e32 v16, v2
	v_mov_b32_e32 v17, v2
	v_mov_b32_e32 v18, v2
	v_mov_b32_e32 v19, v2
	v_mov_b32_e32 v20, v2
	v_mov_b32_e32 v21, v2
	v_mov_b32_e32 v22, v2
	v_mov_b32_e32 v23, v2
	v_mov_b32_e32 v24, v2
	v_mov_b32_e32 v25, v2
	v_mov_b32_e32 v26, v2
	v_mov_b32_e32 v27, v2
	v_mov_b32_e32 v28, v2
	v_mov_b32_e32 v29, v2
	v_mov_b32_e32 v30, v2
	v_mov_b32_e32 v31, v2
	v_mov_b32_e32 v32, v2
	v_mov_b32_e32 v33, v2
	v_mov_b32_e32 v34, v2
	v_mov_b32_e32 v35, v2
	v_mov_b32_e32 v36, v2
	v_mov_b32_e32 v37, v2
	v_mov_b32_e32 v38, v2
	v_mov_b32_e32 v39, v2
	v_mov_b32_e32 v40, v2
	v_mov_b32_e32 v41, v2
	v_mov_b32_e32 v42, v2
	v_mov_b32_e32 v43, v2
	v_mov_b32_e32 v44, v2
	v_mov_b32_e32 v45, v2
	v_mov_b32_e32 v46, v2
	v_mov_b32_e32 v47, v2
	v_mov_b32_e32 v48, v2
	v_mov_b32_e32 v49, v2
	v_mov_b32_e32 v50, v2
	v_mov_b32_e32 v51, v2
	v_mov_b32_e32 v52, v2
	v_mov_b32_e32 v53, v2
	v_mov_b32_e32 v54, v2
	v_mov_b32_e32 v55, v2
	v_mov_b32_e32 v56, v2
	v_mov_b32_e32 v57, v2
	v_mov_b32_e32 v58, v2
	v_mov_b32_e32 v59, v2
	v_mov_b32_e32 v60, v2
	v_mov_b32_e32 v61, v2
	v_mov_b32_e32 v62, v2
	v_mov_b32_e32 v63, v2
	v_mov_b32_e32 v64, v2
	v_mov_b32_e32 v65, v2
	v_readfirstlane_b32 s98, v250
	s_lshr_b32 s99, s98, 2
	s_xor_b32 s98, s98, s99
	s_bitcmp1_b32 s98, 6
	s_cbranch_scc1 .Lmoe_B_1087

.Lp9pf_t1:
	s_or_b64 exec, exec, s[100:101]
	s_waitcnt vmcnt(6)
	s_nop 0
	v_cvt_pk_bf16_f32 v2, v2, v6
	ds_write_b32 v167, v2 offset:49152
	v_cvt_pk_bf16_f32 v2, v3, v7
	ds_write_b32 v167, v2 offset:49216
	v_cvt_pk_bf16_f32 v2, v4, v8
	ds_write_b32 v167, v2 offset:49280
	v_cvt_pk_bf16_f32 v2, v5, v9
	ds_write_b32 v167, v2 offset:49344
	global_load_dwordx4 v[138:141], v[138:139], off sc1 nt
	global_load_dwordx4 v[142:145], v[142:143], off sc1 nt
	s_waitcnt vmcnt(6)
	s_mov_b32 m0, s41
	s_waitcnt lgkmcnt(0)
	s_barrier
	global_load_lds_dwordx4 v146, s[16:17]
	s_mov_b32 m0, s44
	v_mov_b32_e32 v66, 0
	global_load_lds_dwordx4 v156, s[16:17]
	s_mov_b32 s36, -2
	s_movk_i32 s35, 0x80
	v_mov_b32_e32 v67, v66
	v_mov_b32_e32 v68, v66
	v_mov_b32_e32 v69, v66
	v_mov_b32_e32 v70, v66
	v_mov_b32_e32 v71, v66
	v_mov_b32_e32 v72, v66
	v_mov_b32_e32 v73, v66
	v_mov_b32_e32 v74, v66
	v_mov_b32_e32 v75, v66
	v_mov_b32_e32 v76, v66
	v_mov_b32_e32 v77, v66
	v_mov_b32_e32 v78, v66
	v_mov_b32_e32 v79, v66
	v_mov_b32_e32 v80, v66
	v_mov_b32_e32 v81, v66
	v_mov_b32_e32 v82, v66
	v_mov_b32_e32 v83, v66
	v_mov_b32_e32 v84, v66
	v_mov_b32_e32 v85, v66
	v_mov_b32_e32 v86, v66
	v_mov_b32_e32 v87, v66
	v_mov_b32_e32 v88, v66
	v_mov_b32_e32 v89, v66
	v_mov_b32_e32 v90, v66
	v_mov_b32_e32 v91, v66
	v_mov_b32_e32 v92, v66
	v_mov_b32_e32 v93, v66
	v_mov_b32_e32 v94, v66
	v_mov_b32_e32 v95, v66
	v_mov_b32_e32 v96, v66
	v_mov_b32_e32 v97, v66
	v_mov_b32_e32 v98, v66
	v_mov_b32_e32 v99, v66
	v_mov_b32_e32 v100, v66
	v_mov_b32_e32 v101, v66
	v_mov_b32_e32 v102, v66
	v_mov_b32_e32 v103, v66
	v_mov_b32_e32 v104, v66
	v_mov_b32_e32 v105, v66
	v_mov_b32_e32 v106, v66
	v_mov_b32_e32 v107, v66
	v_mov_b32_e32 v108, v66
	v_mov_b32_e32 v109, v66
	v_mov_b32_e32 v110, v66
	v_mov_b32_e32 v111, v66
	v_mov_b32_e32 v112, v66
	v_mov_b32_e32 v113, v66
	v_mov_b32_e32 v114, v66
	v_mov_b32_e32 v115, v66
	v_mov_b32_e32 v116, v66
	v_mov_b32_e32 v117, v66
	v_mov_b32_e32 v118, v66
	v_mov_b32_e32 v119, v66
	v_mov_b32_e32 v120, v66
	v_mov_b32_e32 v121, v66
	v_mov_b32_e32 v122, v66
	v_mov_b32_e32 v123, v66
	v_mov_b32_e32 v124, v66
	v_mov_b32_e32 v125, v66
	v_mov_b32_e32 v126, v66
	v_mov_b32_e32 v127, v66
	v_mov_b32_e32 v128, v66
	v_mov_b32_e32 v129, v66
	v_mov_b32_e32 v2, v66
	v_mov_b32_e32 v3, v66
	v_mov_b32_e32 v4, v66
	v_mov_b32_e32 v5, v66
	v_mov_b32_e32 v6, v66
	v_mov_b32_e32 v7, v66
	v_mov_b32_e32 v8, v66
	v_mov_b32_e32 v9, v66
	v_mov_b32_e32 v10, v66
	v_mov_b32_e32 v11, v66
	v_mov_b32_e32 v12, v66
	v_mov_b32_e32 v13, v66
	v_mov_b32_e32 v14, v66
	v_mov_b32_e32 v15, v66
	v_mov_b32_e32 v16, v66
	v_mov_b32_e32 v17, v66
	v_mov_b32_e32 v18, v66
	v_mov_b32_e32 v19, v66
	v_mov_b32_e32 v20, v66
	v_mov_b32_e32 v21, v66
	v_mov_b32_e32 v22, v66
	v_mov_b32_e32 v23, v66
	v_mov_b32_e32 v24, v66
	v_mov_b32_e32 v25, v66
	v_mov_b32_e32 v26, v66
	v_mov_b32_e32 v27, v66
	v_mov_b32_e32 v28, v66
	v_mov_b32_e32 v29, v66
	v_mov_b32_e32 v30, v66
	v_mov_b32_e32 v31, v66
	v_mov_b32_e32 v32, v66
	v_mov_b32_e32 v33, v66
	v_mov_b32_e32 v34, v66
	v_mov_b32_e32 v35, v66
	v_mov_b32_e32 v36, v66
	v_mov_b32_e32 v37, v66
	v_mov_b32_e32 v38, v66
	v_mov_b32_e32 v39, v66
	v_mov_b32_e32 v40, v66
	v_mov_b32_e32 v41, v66
	v_mov_b32_e32 v42, v66
	v_mov_b32_e32 v43, v66
	v_mov_b32_e32 v44, v66
	v_mov_b32_e32 v45, v66
	v_mov_b32_e32 v46, v66
	v_mov_b32_e32 v47, v66
	v_mov_b32_e32 v48, v66
	v_mov_b32_e32 v49, v66
	v_mov_b32_e32 v50, v66
	v_mov_b32_e32 v51, v66
	v_mov_b32_e32 v52, v66
	v_mov_b32_e32 v53, v66
	v_mov_b32_e32 v54, v66
	v_mov_b32_e32 v55, v66
	v_mov_b32_e32 v56, v66
	v_mov_b32_e32 v57, v66
	v_mov_b32_e32 v58, v66
	v_mov_b32_e32 v59, v66
	v_mov_b32_e32 v60, v66
	v_mov_b32_e32 v61, v66
	v_mov_b32_e32 v62, v66
	v_mov_b32_e32 v63, v66
	v_mov_b32_e32 v64, v66
	v_mov_b32_e32 v65, v66
	v_readfirstlane_b32 s98, v250
	s_lshr_b32 s99, s98, 2
	s_xor_b32 s98, s98, s99
	s_bitcmp1_b32 s98, 6
	s_cbranch_scc1 .Lmoe_B_1091
